# baseline (speedup 1.0000x reference)
.LBB2_22:
	ds_read_b128 v[170:173], v174
	ds_read_b128 v[180:183], v174 offset:2048
	ds_read_b128 v[202:205], v178
	ds_read_b128 v[206:209], v178 offset:2048
	s_mov_b32 s89, s65
	s_mov_b32 s65, s6
	ds_read_b128 v[162:165], v194
	ds_read_b128 v[150:153], v194 offset:2048
	ds_read_b128 v[166:169], v195
	ds_read_b128 v[154:157], v195 offset:2048
	ds_read_b128 v[146:149], v194 offset:4096
	ds_read_b128 v[138:141], v194 offset:6144
	ds_read_b128 v[158:161], v195 offset:4096
	ds_read_b128 v[142:145], v195 offset:6144
	s_waitcnt vmcnt(14)
	s_mul_i32 s94, s83, s35
	v_cvt_pk_f16_f32 v22, v22, v23
	v_cvt_pk_f16_f32 v23, v24, v25
	v_cvt_pk_f16_f32 v18, v18, v19
	v_cvt_pk_f16_f32 v19, v20, v21
	v_cvt_pk_f16_f32 v14, v14, v15
	v_cvt_pk_f16_f32 v15, v16, v17
	v_cvt_pk_f16_f32 v10, v10, v11
	v_cvt_pk_f16_f32 v11, v12, v13
	ds_write2st64_b64 v201, v[22:23], v[18:19] offset0:32 offset1:40
	ds_write2st64_b64 v201, v[14:15], v[10:11] offset0:48 offset1:56
	s_nop 0
	s_lshl_b32 s6, s90, 6
	s_add_i32 s7, s94, s6
	s_lshl_b32 s7, s7, 2
	s_add_i32 s8, s7, s81
	s_add_i32 s9, s8, s81
	s_add_i32 s10, s9, s81
	buffer_load_dwordx4 v[22:25], v192, s[56:59], s7 offen nt
	buffer_load_dwordx4 v[18:21], v192, s[56:59], s8 offen nt
	buffer_load_dwordx4 v[14:17], v192, s[56:59], s9 offen nt
	buffer_load_dwordx4 v[10:13], v192, s[56:59], s10 offen nt
	s_waitcnt vmcnt(16)
	v_add_u32_e32 v210, s89, v193
	s_mul_i32 s95, s84, s35
	ds_write_b128 v210, v[6:9] offset:32768
	ds_write_b128 v210, v[2:5] offset:40960
	s_add_i32 s93, s95, s6
	s_nop 0
	s_barrier
	s_setprio 1
	s_waitcnt lgkmcnt(11)
	v_mfma_f32_16x16x32_f16 v[134:137], v[170:173], v[162:165], v[134:137]
	v_mfma_f32_16x16x32_f16 v[130:133], v[180:183], v[162:165], v[130:133]
	s_waitcnt lgkmcnt(10)
	v_mfma_f32_16x16x32_f16 v[126:129], v[170:173], v[150:153], v[126:129]
	v_mfma_f32_16x16x32_f16 v[122:125], v[180:183], v[150:153], v[122:125]
	s_waitcnt lgkmcnt(7)
	v_mfma_f32_16x16x32_f16 v[118:121], v[170:173], v[146:149], v[118:121]
	v_mfma_f32_16x16x32_f16 v[114:117], v[180:183], v[146:149], v[114:117]
	s_waitcnt lgkmcnt(6)
	v_mfma_f32_16x16x32_f16 v[110:113], v[170:173], v[138:141], v[110:113]
	v_mfma_f32_16x16x32_f16 v[106:109], v[180:183], v[138:141], v[106:109]
	v_mfma_f32_16x16x32_f16 v[134:137], v[202:205], v[166:169], v[134:137]
	v_mfma_f32_16x16x32_f16 v[130:133], v[206:209], v[166:169], v[130:133]
	v_mfma_f32_16x16x32_f16 v[126:129], v[202:205], v[154:157], v[126:129]
	v_mfma_f32_16x16x32_f16 v[122:125], v[206:209], v[154:157], v[122:125]
	s_waitcnt lgkmcnt(5)
	v_mfma_f32_16x16x32_f16 v[118:121], v[202:205], v[158:161], v[118:121]
	v_mfma_f32_16x16x32_f16 v[114:117], v[206:209], v[158:161], v[114:117]
	s_waitcnt lgkmcnt(4)
	v_mfma_f32_16x16x32_f16 v[110:113], v[202:205], v[142:145], v[110:113]
	v_mfma_f32_16x16x32_f16 v[106:109], v[206:209], v[142:145], v[106:109]
	s_waitcnt lgkmcnt(0)
	s_setprio 0
	s_barrier
	ds_read_b128 v[170:173], v174 offset:16384
	ds_read_b128 v[174:177], v174 offset:18432
	ds_read_b128 v[182:185], v178 offset:16384
	ds_read_b128 v[178:181], v178 offset:18432
	s_waitcnt vmcnt(14)
	s_cmp_lt_u32 s92, 32
	ds_write_b128 v210, v[30:33] offset:49152
	ds_write_b128 v210, v[26:29] offset:57344
	s_waitcnt vmcnt(13)
	s_cbranch_scc0 .LBB2_28
	s_add_i32 s38, s64, s92
	s_lshl_b64 s[60:61], s[38:39], 3
	s_add_u32 s60, s60, s85
	v_cmp_ne_u32_e64 s[6:7], 0, v34
	v_cmp_ne_u32_e64 s[8:9], 0, v35
	v_cmp_ne_u32_e64 s[10:11], 0, v36
	v_cmp_ne_u32_e64 s[12:13], 0, v37
	s_addc_u32 s61, s61, 0
	s_nop 1
	s_and_b64 s[98:99], s[6:7], s[8:9]
	s_and_b64 s[100:101], s[10:11], s[12:13]
	s_and_b64 s[98:99], s[98:99], s[100:101]
	s_cmp_eq_u64 s[98:99], -1
	s_cbranch_scc0 .Lqkv_mslow_0
	s_lshl_b64 s[96:97], s[60:61], 5
	v_lshl_add_u64 v[26:27], v[0:1], 0, s[96:97]
	v_mov_b32_e32 v28, -1
	v_mov_b32_e32 v29, -1
	s_add_u32 s6, s42, s60
	s_addc_u32 s7, s43, s61
	s_mov_b64 exec, 15
	global_store_dwordx2 v[26:27], v[28:29], off
	s_mov_b64 exec, 1
	global_store_byte v187, v187, s[6:7]
	s_mov_b64 exec, -1
	s_branch .LBB2_28

.LBB2_33:
	s_barrier
	s_setprio 1
	s_waitcnt lgkmcnt(5)
	v_mfma_f32_16x16x32_f16 v[102:105], v[170:173], v[162:165], v[102:105]
	s_waitcnt lgkmcnt(4)
	v_mfma_f32_16x16x32_f16 v[98:101], v[174:177], v[162:165], v[98:101]
	v_mfma_f32_16x16x32_f16 v[94:97], v[170:173], v[150:153], v[94:97]
	v_mfma_f32_16x16x32_f16 v[90:93], v[174:177], v[150:153], v[90:93]
	v_mfma_f32_16x16x32_f16 v[86:89], v[170:173], v[146:149], v[86:89]
	v_mfma_f32_16x16x32_f16 v[82:85], v[174:177], v[146:149], v[82:85]
	v_mfma_f32_16x16x32_f16 v[78:81], v[170:173], v[138:141], v[78:81]
	v_mfma_f32_16x16x32_f16 v[74:77], v[174:177], v[138:141], v[74:77]
	s_waitcnt lgkmcnt(3)
	v_mfma_f32_16x16x32_f16 v[102:105], v[182:185], v[166:169], v[102:105]
	s_waitcnt lgkmcnt(2)
	v_mfma_f32_16x16x32_f16 v[98:101], v[178:181], v[166:169], v[98:101]
	v_mfma_f32_16x16x32_f16 v[94:97], v[182:185], v[154:157], v[94:97]
	v_mfma_f32_16x16x32_f16 v[90:93], v[178:181], v[154:157], v[90:93]
	v_mfma_f32_16x16x32_f16 v[86:89], v[182:185], v[158:161], v[86:89]
	v_mfma_f32_16x16x32_f16 v[82:85], v[178:181], v[158:161], v[82:85]
	v_mfma_f32_16x16x32_f16 v[78:81], v[182:185], v[142:145], v[78:81]
	v_mfma_f32_16x16x32_f16 v[74:77], v[178:181], v[142:145], v[74:77]
	s_waitcnt lgkmcnt(0)
	s_setprio 0
	s_barrier
	v_add_u32_e32 v202, s89, v196
	v_add_u32_e32 v203, s89, v186
	ds_read_b128 v[170:173], v202 offset:32768
	ds_read_b128 v[174:177], v202 offset:34816
	ds_read_b128 v[178:181], v203 offset:32768
	ds_read_b128 v[182:185], v203 offset:34816
	ds_read_b128 v[162:165], v194 offset:16384
	ds_read_b128 v[150:153], v194 offset:18432
	ds_read_b128 v[166:169], v195 offset:16384
	ds_read_b128 v[154:157], v195 offset:18432
	ds_read_b128 v[146:149], v194 offset:20480
	ds_read_b128 v[138:141], v194 offset:22528
	ds_read_b128 v[158:161], v195 offset:20480
	ds_read_b128 v[142:145], v195 offset:22528
	s_waitcnt vmcnt(14)
	s_lshl_b32 s86, s90, 6
	v_cvt_pk_f16_f32 v58, v58, v59
	v_cvt_pk_f16_f32 v59, v60, v61
	v_cvt_pk_f16_f32 v54, v54, v55
	v_cvt_pk_f16_f32 v55, v56, v57
	v_cvt_pk_f16_f32 v50, v50, v51
	v_cvt_pk_f16_f32 v51, v52, v53
	v_cvt_pk_f16_f32 v46, v46, v47
	v_cvt_pk_f16_f32 v47, v48, v49
	ds_write2st64_b64 v201, v[58:59], v[54:55] offset1:8
	ds_write2st64_b64 v201, v[50:51], v[46:47] offset0:16 offset1:24
	s_nop 0
	s_add_i32 s6, s94, s86
	s_lshl_b32 s6, s6, 2
	s_add_i32 s7, s6, s81
	s_add_i32 s8, s7, s81
	s_add_i32 s9, s8, s81
	buffer_load_dwordx4 v[58:61], v192, s[56:59], s6 offen nt
	buffer_load_dwordx4 v[54:57], v192, s[56:59], s7 offen nt
	buffer_load_dwordx4 v[50:53], v192, s[56:59], s8 offen nt
	buffer_load_dwordx4 v[46:49], v192, s[56:59], s9 offen nt
	s_waitcnt vmcnt(16)
	v_add_u32_e32 v204, s87, v193
	ds_write_b128 v204, v[42:45] offset:32768
	ds_write_b128 v204, v[38:41] offset:40960
	s_nop 0
	s_barrier
	s_setprio 1
	s_waitcnt lgkmcnt(11)
	v_mfma_f32_16x16x32_f16 v[134:137], v[170:173], v[162:165], v[134:137]
	v_mfma_f32_16x16x32_f16 v[130:133], v[174:177], v[162:165], v[130:133]
	s_waitcnt lgkmcnt(10)
	v_mfma_f32_16x16x32_f16 v[126:129], v[170:173], v[150:153], v[126:129]
	v_mfma_f32_16x16x32_f16 v[122:125], v[174:177], v[150:153], v[122:125]
	s_waitcnt lgkmcnt(7)
	v_mfma_f32_16x16x32_f16 v[118:121], v[170:173], v[146:149], v[118:121]
	v_mfma_f32_16x16x32_f16 v[114:117], v[174:177], v[146:149], v[114:117]
	s_waitcnt lgkmcnt(6)
	v_mfma_f32_16x16x32_f16 v[110:113], v[170:173], v[138:141], v[110:113]
	v_mfma_f32_16x16x32_f16 v[106:109], v[174:177], v[138:141], v[106:109]
	v_mfma_f32_16x16x32_f16 v[134:137], v[178:181], v[166:169], v[134:137]
	v_mfma_f32_16x16x32_f16 v[130:133], v[182:185], v[166:169], v[130:133]
	v_mfma_f32_16x16x32_f16 v[126:129], v[178:181], v[154:157], v[126:129]
	v_mfma_f32_16x16x32_f16 v[122:125], v[182:185], v[154:157], v[122:125]
	s_waitcnt lgkmcnt(5)
	v_mfma_f32_16x16x32_f16 v[118:121], v[178:181], v[158:161], v[118:121]
	v_mfma_f32_16x16x32_f16 v[114:117], v[182:185], v[158:161], v[114:117]
	s_waitcnt lgkmcnt(4)
	v_mfma_f32_16x16x32_f16 v[110:113], v[178:181], v[142:145], v[110:113]
	v_mfma_f32_16x16x32_f16 v[106:109], v[182:185], v[142:145], v[106:109]
	s_waitcnt lgkmcnt(0)
	s_setprio 0
	s_barrier
	ds_read_b128 v[170:173], v202 offset:49152
	ds_read_b128 v[174:177], v202 offset:51200
	ds_read_b128 v[182:185], v203 offset:49152
	ds_read_b128 v[178:181], v203 offset:51200
	s_waitcnt vmcnt(14)
	s_cmp_gt_u32 s92, 30
	ds_write_b128 v204, v[66:69] offset:49152
	ds_write_b128 v204, v[62:65] offset:57344
	s_waitcnt vmcnt(13)
	s_cbranch_scc1 .LBB2_39
	s_add_i32 s38, s64, s92
	s_add_i32 s38, s38, 1
	s_lshl_b64 s[60:61], s[38:39], 3
	s_add_u32 s60, s60, s85
	v_cmp_ne_u32_e64 s[6:7], 0, v70
	v_cmp_ne_u32_e64 s[8:9], 0, v71
	v_cmp_ne_u32_e64 s[10:11], 0, v72
	v_cmp_ne_u32_e64 s[12:13], 0, v73
	s_addc_u32 s61, s61, 0
	s_nop 1
	s_and_b64 s[98:99], s[6:7], s[8:9]
	s_and_b64 s[100:101], s[10:11], s[12:13]
	s_and_b64 s[98:99], s[98:99], s[100:101]
	s_cmp_eq_u64 s[98:99], -1
	s_cbranch_scc0 .Lqkv_mslow_1
	s_lshl_b64 s[94:95], s[60:61], 5
	v_lshl_add_u64 v[62:63], v[0:1], 0, s[94:95]
	v_mov_b32_e32 v64, -1
	v_mov_b32_e32 v65, -1
	s_add_u32 s6, s42, s60
	s_addc_u32 s7, s43, s61
	s_mov_b64 exec, 15
	global_store_dwordx2 v[62:63], v[64:65], off
	s_mov_b64 exec, 1
	global_store_byte v187, v187, s[6:7]
	s_mov_b64 exec, -1
	s_branch .LBB2_39

.LBB2_44:
	s_barrier
	s_setprio 1
	s_waitcnt lgkmcnt(5)
	v_mfma_f32_16x16x32_f16 v[102:105], v[170:173], v[162:165], v[102:105]
	s_waitcnt lgkmcnt(4)
	v_mfma_f32_16x16x32_f16 v[98:101], v[174:177], v[162:165], v[98:101]
	v_mfma_f32_16x16x32_f16 v[94:97], v[170:173], v[150:153], v[94:97]
	v_mfma_f32_16x16x32_f16 v[90:93], v[174:177], v[150:153], v[90:93]
	v_mfma_f32_16x16x32_f16 v[86:89], v[170:173], v[146:149], v[86:89]
	v_mfma_f32_16x16x32_f16 v[82:85], v[174:177], v[146:149], v[82:85]
	v_mfma_f32_16x16x32_f16 v[78:81], v[170:173], v[138:141], v[78:81]
	v_mfma_f32_16x16x32_f16 v[74:77], v[174:177], v[138:141], v[74:77]
	s_waitcnt lgkmcnt(3)
	v_mfma_f32_16x16x32_f16 v[102:105], v[182:185], v[166:169], v[102:105]
	s_waitcnt lgkmcnt(2)
	v_mfma_f32_16x16x32_f16 v[98:101], v[178:181], v[166:169], v[98:101]
	v_mfma_f32_16x16x32_f16 v[94:97], v[182:185], v[154:157], v[94:97]
	v_mfma_f32_16x16x32_f16 v[90:93], v[178:181], v[154:157], v[90:93]
	v_mfma_f32_16x16x32_f16 v[86:89], v[182:185], v[158:161], v[86:89]
	v_mfma_f32_16x16x32_f16 v[82:85], v[178:181], v[158:161], v[82:85]
	v_mfma_f32_16x16x32_f16 v[78:81], v[182:185], v[142:145], v[78:81]
	v_mfma_f32_16x16x32_f16 v[74:77], v[178:181], v[142:145], v[74:77]
	s_waitcnt lgkmcnt(0)
	s_setprio 0
	s_barrier
	s_add_i32 s6, s63, 2
	s_cmp_lg_u32 s6, s82
	s_cbranch_scc1 .LBB2_21
	s_mul_i32 s6, s88, s33
	s_add_i32 s6, s6, s73
	s_abs_i32 s8, s6
	s_mul_hi_u32 s9, s8, s75
	s_mul_i32 s10, s9, s72
	s_ashr_i32 s7, s6, 31
	s_sub_i32 s8, s8, s10
	s_xor_b32 s7, s7, s74
	s_add_i32 s10, s9, 1
	s_sub_i32 s11, s8, s72
	s_cmp_ge_u32 s8, s72
	s_cselect_b32 s9, s10, s9
	s_cselect_b32 s8, s11, s8
	s_add_i32 s10, s9, 1
	s_cmp_ge_u32 s8, s72
	s_cselect_b32 s8, s10, s9
	s_xor_b32 s8, s8, s7
	s_sub_i32 s8, s8, s7
	s_mul_i32 s7, s8, s71
	s_sub_i32 s6, s6, s7
	s_abs_i32 s9, s6
	s_mul_hi_u32 s10, s9, s78
	s_mul_i32 s11, s10, s76
	s_ashr_i32 s7, s6, 31
	s_sub_i32 s9, s9, s11
	s_xor_b32 s7, s7, s77
	s_add_i32 s11, s10, 1
	s_sub_i32 s12, s9, s76
	s_cmp_ge_u32 s9, s76
	s_cselect_b32 s10, s11, s10
	s_cselect_b32 s9, s12, s9
	s_add_i32 s11, s10, 1
	s_cmp_ge_u32 s9, s76
	s_cselect_b32 s9, s11, s10
	s_xor_b32 s9, s9, s7
	s_sub_i32 s10, s9, s7
	s_mul_i32 s7, s10, s70
	s_sub_i32 s11, s6, s7
	s_cmp_eq_u32 s8, 0
	s_cselect_b64 s[6:7], -1, 0
	s_cmp_eq_u32 s8, 1
	v_mov_b32_e32 v139, s46
	v_mov_b32_e32 v140, s45
	s_cselect_b64 s[8:9], -1, 0
	v_mov_b32_e32 v138, s44
	v_cndmask_b32_e64 v139, v139, v140, s[8:9]
	s_and_b64 s[8:9], s[8:9], exec
	v_cndmask_b32_e64 v138, v139, v138, s[6:7]
	s_cselect_b32 s8, s31, s37
	s_cselect_b32 s9, s30, s36
	s_and_b64 s[6:7], s[6:7], exec
	v_pk_mul_f32 v[134:135], v[138:139], v[134:135] op_sel_hi:[0,1]
	v_pk_mul_f32 v[136:137], v[138:139], v[136:137] op_sel_hi:[0,1]
	v_pk_mul_f32 v[130:131], v[138:139], v[130:131] op_sel_hi:[0,1]
	s_cselect_b32 s6, s29, s8
	s_mul_i32 s10, s10, s80
	v_cvt_pk_f16_f32 v134, v134, v135
	v_cvt_pk_f16_f32 v135, v136, v137
	v_cvt_pk_f16_f32 v136, v130, v131
	v_pk_mul_f32 v[130:131], v[138:139], v[132:133] op_sel_hi:[0,1]
	s_cselect_b32 s60, s28, s9
	s_and_b32 s61, s6, 0xffff
	s_lshl_b32 s6, s11, 9
	s_lshl_b32 s7, s10, 7
	v_cvt_pk_f16_f32 v137, v130, v131
	v_pk_mul_f32 v[126:127], v[138:139], v[126:127] op_sel_hi:[0,1]
	v_pk_mul_f32 v[128:129], v[138:139], v[128:129] op_sel_hi:[0,1]
	v_pk_mul_f32 v[122:123], v[138:139], v[122:123] op_sel_hi:[0,1]
	s_mov_b32 s63, s15
	s_add_i32 s8, s6, s7
	v_permlane16_swap_b32_e32 v134, v136
	v_permlane16_swap_b32_e32 v135, v137
	v_cvt_pk_f16_f32 v126, v126, v127
	v_cvt_pk_f16_f32 v127, v128, v129
	v_cvt_pk_f16_f32 v128, v122, v123
	v_pk_mul_f32 v[122:123], v[138:139], v[124:125] op_sel_hi:[0,1]
	buffer_store_dwordx4 v[134:137], v199, s[60:63], s8 offen
	s_add_i32 s8, s7, s34
	v_cvt_pk_f16_f32 v129, v122, v123
	v_pk_mul_f32 v[118:119], v[138:139], v[118:119] op_sel_hi:[0,1]
	v_pk_mul_f32 v[120:121], v[138:139], v[120:121] op_sel_hi:[0,1]
	v_pk_mul_f32 v[114:115], v[138:139], v[114:115] op_sel_hi:[0,1]
	s_add_i32 s9, s6, s8
	v_permlane16_swap_b32_e32 v126, v128
	v_permlane16_swap_b32_e32 v127, v129
	v_cvt_pk_f16_f32 v118, v118, v119
	v_cvt_pk_f16_f32 v119, v120, v121
	v_cvt_pk_f16_f32 v120, v114, v115
	v_pk_mul_f32 v[114:115], v[138:139], v[116:117] op_sel_hi:[0,1]
	buffer_store_dwordx4 v[126:129], v199, s[60:63], s9 offen
	s_add_i32 s9, s8, s34
	v_cvt_pk_f16_f32 v121, v114, v115
	s_add_i32 s10, s6, s9
	v_permlane16_swap_b32_e32 v118, v120
	v_permlane16_swap_b32_e32 v119, v121
	v_pk_mul_f32 v[110:111], v[138:139], v[110:111] op_sel_hi:[0,1]
	v_pk_mul_f32 v[112:113], v[138:139], v[112:113] op_sel_hi:[0,1]
	v_pk_mul_f32 v[106:107], v[138:139], v[106:107] op_sel_hi:[0,1]
	v_pk_mul_f32 v[102:103], v[138:139], v[102:103] op_sel_hi:[0,1]
	v_pk_mul_f32 v[104:105], v[138:139], v[104:105] op_sel_hi:[0,1]
	v_pk_mul_f32 v[98:99], v[138:139], v[98:99] op_sel_hi:[0,1]
	buffer_store_dwordx4 v[118:121], v199, s[60:63], s10 offen
	s_add_i32 s10, s9, s34
	v_cvt_pk_f16_f32 v110, v110, v111
	v_cvt_pk_f16_f32 v111, v112, v113
	v_cvt_pk_f16_f32 v112, v106, v107
	v_pk_mul_f32 v[106:107], v[138:139], v[108:109] op_sel_hi:[0,1]
	v_cvt_pk_f16_f32 v102, v102, v103
	v_cvt_pk_f16_f32 v103, v104, v105
	v_cvt_pk_f16_f32 v104, v98, v99
	v_pk_mul_f32 v[98:99], v[138:139], v[100:101] op_sel_hi:[0,1]
	v_pk_mul_f32 v[94:95], v[138:139], v[94:95] op_sel_hi:[0,1]
	v_pk_mul_f32 v[96:97], v[138:139], v[96:97] op_sel_hi:[0,1]
	v_pk_mul_f32 v[90:91], v[138:139], v[90:91] op_sel_hi:[0,1]
	s_add_i32 s11, s6, s10
	v_cvt_pk_f16_f32 v113, v106, v107
	s_bitset1_b32 s6, 8
	v_cvt_pk_f16_f32 v105, v98, v99
	v_cvt_pk_f16_f32 v94, v94, v95
	v_cvt_pk_f16_f32 v95, v96, v97
	v_cvt_pk_f16_f32 v96, v90, v91
	v_pk_mul_f32 v[90:91], v[138:139], v[92:93] op_sel_hi:[0,1]
	v_pk_mul_f32 v[86:87], v[138:139], v[86:87] op_sel_hi:[0,1]
	v_pk_mul_f32 v[88:89], v[138:139], v[88:89] op_sel_hi:[0,1]
	v_pk_mul_f32 v[82:83], v[138:139], v[82:83] op_sel_hi:[0,1]
	v_pk_mul_f32 v[78:79], v[138:139], v[78:79] op_sel_hi:[0,1]
	v_pk_mul_f32 v[80:81], v[138:139], v[80:81] op_sel_hi:[0,1]
	v_pk_mul_f32 v[74:75], v[138:139], v[74:75] op_sel_hi:[0,1]
	v_permlane16_swap_b32_e32 v110, v112
	v_permlane16_swap_b32_e32 v111, v113
	s_add_i32 s7, s6, s7
	v_permlane16_swap_b32_e32 v102, v104
	v_permlane16_swap_b32_e32 v103, v105
	v_cvt_pk_f16_f32 v97, v90, v91
	v_cvt_pk_f16_f32 v86, v86, v87
	v_cvt_pk_f16_f32 v87, v88, v89
	v_cvt_pk_f16_f32 v88, v82, v83
	v_pk_mul_f32 v[82:83], v[138:139], v[84:85] op_sel_hi:[0,1]
	v_cvt_pk_f16_f32 v78, v78, v79
	v_cvt_pk_f16_f32 v79, v80, v81
	v_cvt_pk_f16_f32 v80, v74, v75
	v_pk_mul_f32 v[74:75], v[138:139], v[76:77] op_sel_hi:[0,1]
	buffer_store_dwordx4 v[110:113], v199, s[60:63], s11 offen
	buffer_store_dwordx4 v[102:105], v199, s[60:63], s7 offen
	s_add_i32 s7, s6, s8
	v_permlane16_swap_b32_e32 v94, v96
	v_permlane16_swap_b32_e32 v95, v97
	v_cvt_pk_f16_f32 v89, v82, v83
	v_cvt_pk_f16_f32 v81, v74, v75
	buffer_store_dwordx4 v[94:97], v199, s[60:63], s7 offen
	s_add_i32 s7, s6, s9
	v_permlane16_swap_b32_e32 v86, v88
	v_permlane16_swap_b32_e32 v87, v89
	s_add_i32 s6, s6, s10
	v_permlane16_swap_b32_e32 v78, v80
	v_permlane16_swap_b32_e32 v79, v81
	v_mov_b32_e32 v74, 0
	buffer_store_dwordx4 v[86:89], v199, s[60:63], s7 offen
	buffer_store_dwordx4 v[78:81], v199, s[60:63], s6 offen
	s_add_i32 s88, s88, 1
	s_mov_b32 s63, -2
	v_mov_b32_e32 v75, v74
	v_mov_b32_e32 v76, v74
	v_mov_b32_e32 v77, v74
	v_mov_b32_e32 v78, v74
	v_mov_b32_e32 v79, v74
	v_mov_b32_e32 v80, v74
	v_mov_b32_e32 v81, v74
	v_mov_b32_e32 v82, v74
	v_mov_b32_e32 v83, v74
	v_mov_b32_e32 v84, v74
	v_mov_b32_e32 v85, v74
	v_mov_b32_e32 v86, v74
	v_mov_b32_e32 v87, v74
	v_mov_b32_e32 v88, v74
	v_mov_b32_e32 v89, v74
	v_mov_b32_e32 v90, v74
	v_mov_b32_e32 v91, v74
	v_mov_b32_e32 v92, v74
	v_mov_b32_e32 v93, v74
	v_mov_b32_e32 v94, v74
	v_mov_b32_e32 v95, v74
	v_mov_b32_e32 v96, v74
	v_mov_b32_e32 v97, v74
	v_mov_b32_e32 v98, v74
	v_mov_b32_e32 v99, v74
	v_mov_b32_e32 v100, v74
	v_mov_b32_e32 v101, v74
	v_mov_b32_e32 v102, v74
	v_mov_b32_e32 v103, v74
	v_mov_b32_e32 v104, v74
	v_mov_b32_e32 v105, v74
	v_mov_b32_e32 v106, v74
	v_mov_b32_e32 v107, v74
	v_mov_b32_e32 v108, v74
	v_mov_b32_e32 v109, v74
	v_mov_b32_e32 v110, v74
	v_mov_b32_e32 v111, v74
	v_mov_b32_e32 v112, v74
	v_mov_b32_e32 v113, v74
	v_mov_b32_e32 v114, v74
	v_mov_b32_e32 v115, v74
	v_mov_b32_e32 v116, v74
	v_mov_b32_e32 v117, v74
	v_mov_b32_e32 v118, v74
	v_mov_b32_e32 v119, v74
	v_mov_b32_e32 v120, v74
	v_mov_b32_e32 v121, v74
	v_mov_b32_e32 v122, v74
	v_mov_b32_e32 v123, v74
	v_mov_b32_e32 v124, v74
	v_mov_b32_e32 v125, v74
	v_mov_b32_e32 v126, v74
	v_mov_b32_e32 v127, v74
	v_mov_b32_e32 v128, v74
	v_mov_b32_e32 v129, v74
	v_mov_b32_e32 v130, v74
	v_mov_b32_e32 v131, v74
	v_mov_b32_e32 v132, v74
	v_mov_b32_e32 v133, v74
	v_mov_b32_e32 v134, v74
	v_mov_b32_e32 v135, v74
	v_mov_b32_e32 v136, v74
	v_mov_b32_e32 v137, v74
	s_branch .LBB2_21
